# v_X plus P.V MFMA pairs of the attention loops ordered so consecutive pairs share the P fragment
# speedup vs baseline: 1.0082x; 1.0032x over previous
.LBB0_917:
	v_cmp_neq_f32_e32 vcc, s41, v226
	s_nop 1
	v_cndmask_b32_e32 v126, 0, v226, vcc
	v_sub_f32_e32 v114, v114, v126
	v_exp_f32_e32 v127, v114
	v_sub_f32_e32 v114, v115, v126
	v_exp_f32_e32 v129, v114
	v_sub_f32_e32 v114, v116, v126
	v_exp_f32_e32 v135, v114
	v_sub_f32_e32 v114, v117, v126
	v_exp_f32_e32 v137, v114
	v_sub_f32_e32 v114, v118, v126
	v_exp_f32_e32 v143, v114
	v_sub_f32_e32 v114, v119, v126
	v_exp_f32_e32 v145, v114
	v_sub_f32_e32 v114, v120, v126
	v_exp_f32_e32 v151, v114
	v_sub_f32_e32 v114, v121, v126
	v_exp_f32_e32 v153, v114
	v_sub_f32_e32 v114, v122, v126
	v_exp_f32_e32 v159, v114
	v_sub_f32_e32 v114, v123, v126
	v_exp_f32_e32 v161, v114
	v_sub_f32_e32 v114, v124, v126
	v_exp_f32_e32 v167, v114
	v_sub_f32_e32 v114, v125, v126
	v_exp_f32_e32 v169, v114
	v_sub_f32_e32 v114, v130, v126
	v_exp_f32_e32 v171, v114
	v_sub_f32_e32 v114, v131, v126
	v_exp_f32_e32 v131, v114
	v_sub_f32_e32 v114, v132, v126
	v_cmp_neq_f32_e32 vcc, s41, v225
	v_exp_f32_e32 v173, v114
	v_sub_f32_e32 v114, v133, v126
	v_cndmask_b32_e32 v117, 0, v225, vcc
	v_exp_f32_e32 v133, v114
	v_sub_f32_e32 v114, v138, v117
	v_exp_f32_e32 v126, v114
	v_sub_f32_e32 v114, v139, v117
	v_exp_f32_e32 v128, v114
	v_sub_f32_e32 v114, v140, v117
	v_exp_f32_e32 v134, v114
	v_sub_f32_e32 v114, v141, v117
	v_exp_f32_e32 v136, v114
	v_sub_f32_e32 v114, v146, v117
	v_exp_f32_e32 v142, v114
	v_sub_f32_e32 v114, v147, v117
	v_pk_add_f32 v[118:119], v[126:127], 0 op_sel_hi:[1,0]
	v_exp_f32_e32 v144, v114
	v_pk_add_f32 v[118:119], v[128:129], v[118:119]
	v_sub_f32_e32 v120, v148, v117
	v_pk_add_f32 v[118:119], v[134:135], v[118:119]
	v_exp_f32_e32 v150, v120
	v_sub_f32_e32 v120, v149, v117
	v_pk_add_f32 v[118:119], v[136:137], v[118:119]
	v_exp_f32_e32 v152, v120
	v_sub_f32_e32 v120, v154, v117
	v_pk_add_f32 v[118:119], v[142:143], v[118:119]
	v_exp_f32_e32 v158, v120
	v_sub_f32_e32 v120, v155, v117
	v_pk_add_f32 v[118:119], v[144:145], v[118:119]
	v_exp_f32_e32 v160, v120
	v_sub_f32_e32 v120, v156, v117
	v_exp_f32_e32 v166, v120
	v_sub_f32_e32 v120, v157, v117
	v_pk_add_f32 v[118:119], v[150:151], v[118:119]
	v_exp_f32_e32 v168, v120
	v_sub_f32_e32 v120, v162, v117
	v_pk_add_f32 v[118:119], v[152:153], v[118:119]
	v_exp_f32_e32 v170, v120
	v_sub_f32_e32 v120, v163, v117
	v_pk_add_f32 v[118:119], v[158:159], v[118:119]
	v_exp_f32_e32 v130, v120
	v_sub_f32_e32 v120, v164, v117
	v_pk_add_f32 v[118:119], v[160:161], v[118:119]
	v_exp_f32_e32 v172, v120
	v_sub_f32_e32 v117, v165, v117
	v_pk_add_f32 v[118:119], v[166:167], v[118:119]
	v_exp_f32_e32 v132, v117
	v_pk_add_f32 v[118:119], v[168:169], v[118:119]
	v_add3_u32 v146, s84, v207, v208
	v_pk_add_f32 v[118:119], v[170:171], v[118:119]
	v_cvt_pk_bf16_f32 v114, v127, v129
	v_cvt_pk_bf16_f32 v115, v135, v137
	v_cvt_pk_bf16_f32 v116, v143, v145
	v_cvt_pk_bf16_f32 v117, v151, v153
	s_nop 0
	v_pk_add_f32 v[118:119], v[130:131], v[118:119]
	s_nop 0
	v_pk_add_f32 v[118:119], v[172:173], v[118:119]
	s_nop 0
	v_pk_add_f32 v[122:123], v[132:133], v[118:119]
	v_cvt_pk_bf16_f32 v118, v159, v161
	v_cvt_pk_bf16_f32 v119, v167, v169
	v_cvt_pk_bf16_f32 v120, v171, v131
	v_cvt_pk_bf16_f32 v121, v173, v133
	s_nop 0
	v_pk_add_f32 v[194:195], v[194:195], v[122:123]
	v_cvt_pk_bf16_f32 v122, v126, v128
	v_cvt_pk_bf16_f32 v123, v134, v136
	v_cvt_pk_bf16_f32 v124, v142, v144
	v_cvt_pk_bf16_f32 v125, v150, v152
	v_cvt_pk_bf16_f32 v126, v158, v160
	v_cvt_pk_bf16_f32 v127, v166, v168
	v_cvt_pk_bf16_f32 v128, v170, v130
	v_cvt_pk_bf16_f32 v129, v172, v132
	ds_read_b64_tr_b16 v[132:133], v146 offset:23040
	ds_read_b64_tr_b16 v[130:131], v146 offset:18432
	ds_read_b64_tr_b16 v[134:135], v146 offset:18464
	ds_read_b64_tr_b16 v[136:137], v146 offset:23072
	ds_read_b64_tr_b16 v[138:139], v146 offset:18496
	ds_read_b64_tr_b16 v[140:141], v146 offset:23104
	ds_read_b64_tr_b16 v[142:143], v146 offset:18528
	ds_read_b64_tr_b16 v[144:145], v146 offset:23136
	s_setprio 2
	s_waitcnt lgkmcnt(6)
	v_mfma_f32_16x16x32_bf16 v[110:113], v[130:133], v[114:117], v[110:113]
	v_mfma_f32_16x16x32_bf16 v[78:81], v[130:133], v[122:125], v[78:81]
	s_waitcnt lgkmcnt(4)
	v_mfma_f32_16x16x32_bf16 v[74:77], v[134:137], v[122:125], v[74:77]
	v_mfma_f32_16x16x32_bf16 v[106:109], v[134:137], v[114:117], v[106:109]
	s_setprio 0
	ds_read_b64_tr_b16 v[132:133], v146 offset:23168
	ds_read_b64_tr_b16 v[130:131], v146 offset:18560
	ds_read_b64_tr_b16 v[136:137], v146 offset:23200
	ds_read_b64_tr_b16 v[134:135], v146 offset:18592
	s_setprio 2
	s_waitcnt lgkmcnt(6)
	v_mfma_f32_16x16x32_bf16 v[102:105], v[138:141], v[114:117], v[102:105]
	v_mfma_f32_16x16x32_bf16 v[70:73], v[138:141], v[122:125], v[70:73]
	s_waitcnt lgkmcnt(4)
	v_mfma_f32_16x16x32_bf16 v[66:69], v[142:145], v[122:125], v[66:69]
	v_mfma_f32_16x16x32_bf16 v[98:101], v[142:145], v[114:117], v[98:101]
	s_setprio 0
	ds_read_b64_tr_b16 v[140:141], v146 offset:23232
	ds_read_b64_tr_b16 v[138:139], v146 offset:18624
	ds_read_b64_tr_b16 v[144:145], v146 offset:23264
	ds_read_b64_tr_b16 v[142:143], v146 offset:18656
	s_setprio 2
	s_waitcnt lgkmcnt(6)
	v_mfma_f32_16x16x32_bf16 v[94:97], v[130:133], v[114:117], v[94:97]
	v_mfma_f32_16x16x32_bf16 v[62:65], v[130:133], v[122:125], v[62:65]
	s_waitcnt lgkmcnt(4)
	v_mfma_f32_16x16x32_bf16 v[58:61], v[134:137], v[122:125], v[58:61]
	v_mfma_f32_16x16x32_bf16 v[90:93], v[134:137], v[114:117], v[90:93]
	s_setprio 0
	ds_read_b64_tr_b16 v[132:133], v146 offset:32256
	ds_read_b64_tr_b16 v[130:131], v146 offset:27648
	ds_read_b64_tr_b16 v[136:137], v146 offset:32288
	ds_read_b64_tr_b16 v[134:135], v146 offset:27680
	s_setprio 2
	s_waitcnt lgkmcnt(6)
	v_mfma_f32_16x16x32_bf16 v[86:89], v[138:141], v[114:117], v[86:89]
	v_mfma_f32_16x16x32_bf16 v[54:57], v[138:141], v[122:125], v[54:57]
	s_waitcnt lgkmcnt(4)
	v_mfma_f32_16x16x32_bf16 v[50:53], v[142:145], v[122:125], v[50:53]
	v_mfma_f32_16x16x32_bf16 v[82:85], v[142:145], v[114:117], v[82:85]
	s_setprio 0
	ds_read_b64_tr_b16 v[116:117], v146 offset:32320
	ds_read_b64_tr_b16 v[114:115], v146 offset:27712
	ds_read_b64_tr_b16 v[124:125], v146 offset:32352
	ds_read_b64_tr_b16 v[122:123], v146 offset:27744
	s_setprio 2
	s_waitcnt lgkmcnt(6)
	v_mfma_f32_16x16x32_bf16 v[110:113], v[130:133], v[118:121], v[110:113]
	v_mfma_f32_16x16x32_bf16 v[78:81], v[130:133], v[126:129], v[78:81]
	s_waitcnt lgkmcnt(4)
	v_mfma_f32_16x16x32_bf16 v[74:77], v[134:137], v[126:129], v[74:77]
	v_mfma_f32_16x16x32_bf16 v[106:109], v[134:137], v[118:121], v[106:109]
	s_setprio 0
	ds_read_b64_tr_b16 v[132:133], v146 offset:32384
	ds_read_b64_tr_b16 v[130:131], v146 offset:27776
	ds_read_b64_tr_b16 v[136:137], v146 offset:32416
	ds_read_b64_tr_b16 v[134:135], v146 offset:27808
	s_setprio 2
	s_waitcnt lgkmcnt(6)
	v_mfma_f32_16x16x32_bf16 v[102:105], v[114:117], v[118:121], v[102:105]
	v_mfma_f32_16x16x32_bf16 v[70:73], v[114:117], v[126:129], v[70:73]
	s_waitcnt lgkmcnt(4)
	v_mfma_f32_16x16x32_bf16 v[66:69], v[122:125], v[126:129], v[66:69]
	v_mfma_f32_16x16x32_bf16 v[98:101], v[122:125], v[118:121], v[98:101]
	s_setprio 0
	ds_read_b64_tr_b16 v[116:117], v146 offset:32448
	ds_read_b64_tr_b16 v[114:115], v146 offset:27840
	ds_read_b64_tr_b16 v[124:125], v146 offset:32480
	ds_read_b64_tr_b16 v[122:123], v146 offset:27872
	s_setprio 2
	s_waitcnt lgkmcnt(6)
	v_mfma_f32_16x16x32_bf16 v[94:97], v[130:133], v[118:121], v[94:97]
	v_mfma_f32_16x16x32_bf16 v[62:65], v[130:133], v[126:129], v[62:65]
	s_waitcnt lgkmcnt(4)
	v_mfma_f32_16x16x32_bf16 v[58:61], v[134:137], v[126:129], v[58:61]
	v_mfma_f32_16x16x32_bf16 v[90:93], v[134:137], v[118:121], v[90:93]
	s_setprio 0
	s_setprio 2
	s_waitcnt lgkmcnt(2)
	v_mfma_f32_16x16x32_bf16 v[86:89], v[114:117], v[118:121], v[86:89]
	v_mfma_f32_16x16x32_bf16 v[54:57], v[114:117], v[126:129], v[54:57]
	s_waitcnt lgkmcnt(0)
	v_mfma_f32_16x16x32_bf16 v[50:53], v[122:125], v[126:129], v[50:53]
	v_mfma_f32_16x16x32_bf16 v[82:85], v[122:125], v[118:121], v[82:85]
	s_setprio 0

.LBB0_935:
	v_cmp_neq_f32_e32 vcc, s41, v153
	s_nop 1
	v_cndmask_b32_e32 v114, 0, v153, vcc
	v_sub_f32_e32 v115, v161, v114
	v_exp_f32_e32 v123, v115
	v_sub_f32_e32 v115, v162, v114
	v_exp_f32_e32 v125, v115
	v_sub_f32_e32 v115, v164, v114
	v_exp_f32_e32 v127, v115
	v_sub_f32_e32 v115, v165, v114
	v_exp_f32_e32 v129, v115
	v_sub_f32_e32 v115, v166, v114
	v_exp_f32_e32 v165, v115
	v_sub_f32_e32 v115, v169, v114
	v_exp_f32_e32 v187, v115
	v_sub_f32_e32 v115, v170, v114
	v_exp_f32_e32 v189, v115
	v_sub_f32_e32 v115, v173, v114
	v_cmp_neq_f32_e32 vcc, s41, v152
	v_exp_f32_e32 v191, v115
	v_sub_f32_e32 v115, v174, v114
	v_cndmask_b32_e32 v162, 0, v152, vcc
	v_exp_f32_e32 v193, v115
	v_sub_f32_e32 v115, v175, v114
	v_sub_f32_e32 v122, v133, v162
	v_exp_f32_e32 v175, v115
	v_sub_f32_e32 v115, v176, v114
	v_exp_f32_e32 v122, v122
	v_sub_f32_e32 v124, v183, v162
	v_exp_f32_e32 v161, v115
	v_sub_f32_e32 v115, v177, v114
	v_exp_f32_e32 v124, v124
	v_sub_f32_e32 v126, v184, v162
	v_exp_f32_e32 v177, v115
	v_sub_f32_e32 v115, v179, v114
	v_exp_f32_e32 v126, v126
	v_sub_f32_e32 v128, v185, v162
	v_exp_f32_e32 v195, v115
	v_sub_f32_e32 v115, v130, v114
	v_exp_f32_e32 v128, v128
	v_sub_f32_e32 v130, v154, v162
	v_exp_f32_e32 v169, v115
	v_sub_f32_e32 v115, v131, v114
	v_sub_f32_e32 v114, v132, v114
	v_exp_f32_e32 v164, v130
	v_sub_f32_e32 v130, v156, v162
	v_pk_add_f32 v[132:133], v[122:123], 0 op_sel_hi:[1,0]
	v_cvt_pk_bf16_f32 v118, v123, v125
	v_exp_f32_e32 v186, v130
	v_pk_add_f32 v[132:133], v[124:125], v[132:133]
	v_sub_f32_e32 v123, v155, v162
	v_pk_add_f32 v[132:133], v[126:127], v[132:133]
	v_exp_f32_e32 v188, v123
	v_sub_f32_e32 v123, v157, v162
	v_pk_add_f32 v[132:133], v[128:129], v[132:133]
	v_exp_f32_e32 v190, v123
	v_sub_f32_e32 v123, v158, v162
	v_pk_add_f32 v[132:133], v[164:165], v[132:133]
	v_exp_f32_e32 v192, v123
	v_sub_f32_e32 v123, v159, v162
	v_pk_add_f32 v[132:133], v[186:187], v[132:133]
	v_exp_f32_e32 v174, v123
	v_sub_f32_e32 v123, v160, v162
	v_exp_f32_e32 v160, v123
	v_sub_f32_e32 v123, v163, v162
	v_pk_add_f32 v[132:133], v[188:189], v[132:133]
	v_exp_f32_e32 v176, v123
	v_sub_f32_e32 v123, v167, v162
	v_pk_add_f32 v[132:133], v[190:191], v[132:133]
	v_exp_f32_e32 v194, v123
	v_sub_f32_e32 v123, v168, v162
	v_pk_add_f32 v[132:133], v[192:193], v[132:133]
	v_exp_f32_e32 v168, v123
	v_sub_f32_e32 v123, v171, v162
	v_pk_add_f32 v[132:133], v[174:175], v[132:133]
	v_exp_f32_e32 v131, v115
	v_exp_f32_e32 v130, v123
	v_sub_f32_e32 v123, v172, v162
	v_pk_add_f32 v[132:133], v[160:161], v[132:133]
	v_exp_f32_e32 v173, v114
	v_exp_f32_e32 v172, v123
	v_pk_add_f32 v[132:133], v[176:177], v[132:133]
	v_add3_u32 v166, s63, v149, v150
	v_pk_add_f32 v[132:133], v[194:195], v[132:133]
	v_cvt_pk_bf16_f32 v119, v127, v129
	v_cvt_pk_bf16_f32 v120, v165, v187
	v_cvt_pk_bf16_f32 v121, v189, v191
	v_cvt_pk_bf16_f32 v114, v193, v175
	v_cvt_pk_bf16_f32 v115, v161, v177
	s_nop 0
	v_pk_add_f32 v[132:133], v[168:169], v[132:133]
	v_cvt_pk_bf16_f32 v116, v195, v169
	v_cvt_pk_bf16_f32 v117, v131, v173
	v_cvt_pk_bf16_f32 v122, v122, v124
	v_cvt_pk_bf16_f32 v123, v126, v128
	v_cvt_pk_bf16_f32 v124, v164, v186
	s_nop 0
	v_pk_add_f32 v[132:133], v[130:131], v[132:133]
	v_cvt_pk_bf16_f32 v125, v188, v190
	v_cvt_pk_bf16_f32 v126, v192, v174
	v_cvt_pk_bf16_f32 v127, v160, v176
	v_cvt_pk_bf16_f32 v128, v194, v168
	v_cvt_pk_bf16_f32 v129, v130, v172
	s_nop 0
	v_pk_add_f32 v[132:133], v[172:173], v[132:133]
	s_nop 0
	v_pk_add_f32 v[134:135], v[134:135], v[132:133]
	ds_read_b64_tr_b16 v[132:133], v166 offset:23040
	ds_read_b64_tr_b16 v[130:131], v166 offset:18432
	ds_read_b64_tr_b16 v[154:155], v166 offset:18464
	ds_read_b64_tr_b16 v[156:157], v166 offset:23072
	ds_read_b64_tr_b16 v[158:159], v166 offset:18496
	ds_read_b64_tr_b16 v[160:161], v166 offset:23104
	ds_read_b64_tr_b16 v[162:163], v166 offset:18528
	ds_read_b64_tr_b16 v[164:165], v166 offset:23136
	s_setprio 2
	s_waitcnt lgkmcnt(6)
	v_mfma_f32_16x16x32_bf16 v[110:113], v[130:133], v[118:121], v[110:113]
	v_mfma_f32_16x16x32_bf16 v[30:33], v[130:133], v[122:125], v[30:33]
	s_waitcnt lgkmcnt(4)
	v_mfma_f32_16x16x32_bf16 v[26:29], v[154:157], v[122:125], v[26:29]
	v_mfma_f32_16x16x32_bf16 v[106:109], v[154:157], v[118:121], v[106:109]
	s_setprio 0
	ds_read_b64_tr_b16 v[132:133], v166 offset:23168
	ds_read_b64_tr_b16 v[130:131], v166 offset:18560
	ds_read_b64_tr_b16 v[156:157], v166 offset:23200
	ds_read_b64_tr_b16 v[154:155], v166 offset:18592
	s_setprio 2
	s_waitcnt lgkmcnt(6)
	v_mfma_f32_16x16x32_bf16 v[102:105], v[158:161], v[118:121], v[102:105]
	v_mfma_f32_16x16x32_bf16 v[22:25], v[158:161], v[122:125], v[22:25]
	s_waitcnt lgkmcnt(4)
	v_mfma_f32_16x16x32_bf16 v[18:21], v[162:165], v[122:125], v[18:21]
	v_mfma_f32_16x16x32_bf16 v[98:101], v[162:165], v[118:121], v[98:101]
	s_setprio 0
	ds_read_b64_tr_b16 v[160:161], v166 offset:23232
	ds_read_b64_tr_b16 v[158:159], v166 offset:18624
	ds_read_b64_tr_b16 v[164:165], v166 offset:23264
	ds_read_b64_tr_b16 v[162:163], v166 offset:18656
	s_setprio 2
	s_waitcnt lgkmcnt(6)
	v_mfma_f32_16x16x32_bf16 v[94:97], v[130:133], v[118:121], v[94:97]
	v_mfma_f32_16x16x32_bf16 v[14:17], v[130:133], v[122:125], v[14:17]
	s_waitcnt lgkmcnt(4)
	v_mfma_f32_16x16x32_bf16 v[10:13], v[154:157], v[122:125], v[10:13]
	v_mfma_f32_16x16x32_bf16 v[86:89], v[154:157], v[118:121], v[86:89]
	s_setprio 0
	ds_read_b64_tr_b16 v[132:133], v166 offset:32256
	ds_read_b64_tr_b16 v[130:131], v166 offset:27648
	ds_read_b64_tr_b16 v[156:157], v166 offset:32288
	ds_read_b64_tr_b16 v[154:155], v166 offset:27680
	s_setprio 2
	s_waitcnt lgkmcnt(6)
	v_mfma_f32_16x16x32_bf16 v[70:73], v[158:161], v[118:121], v[70:73]
	v_mfma_f32_16x16x32_bf16 v[6:9], v[158:161], v[122:125], v[6:9]
	s_waitcnt lgkmcnt(4)
	v_mfma_f32_16x16x32_bf16 v[2:5], v[162:165], v[122:125], v[2:5]
	v_mfma_f32_16x16x32_bf16 v[66:69], v[162:165], v[118:121], v[66:69]
	s_setprio 0
	ds_read_b64_tr_b16 v[120:121], v166 offset:32320
	ds_read_b64_tr_b16 v[118:119], v166 offset:27712
	ds_read_b64_tr_b16 v[124:125], v166 offset:32352
	ds_read_b64_tr_b16 v[122:123], v166 offset:27744
	s_setprio 2
	s_waitcnt lgkmcnt(6)
	v_mfma_f32_16x16x32_bf16 v[110:113], v[130:133], v[114:117], v[110:113]
	v_mfma_f32_16x16x32_bf16 v[30:33], v[130:133], v[126:129], v[30:33]
	s_waitcnt lgkmcnt(4)
	v_mfma_f32_16x16x32_bf16 v[26:29], v[154:157], v[126:129], v[26:29]
	v_mfma_f32_16x16x32_bf16 v[106:109], v[154:157], v[114:117], v[106:109]
	s_setprio 0
	ds_read_b64_tr_b16 v[132:133], v166 offset:32384
	ds_read_b64_tr_b16 v[130:131], v166 offset:27776
	ds_read_b64_tr_b16 v[156:157], v166 offset:32416
	ds_read_b64_tr_b16 v[154:155], v166 offset:27808
	s_setprio 2
	s_waitcnt lgkmcnt(6)
	v_mfma_f32_16x16x32_bf16 v[102:105], v[118:121], v[114:117], v[102:105]
	v_mfma_f32_16x16x32_bf16 v[22:25], v[118:121], v[126:129], v[22:25]
	s_waitcnt lgkmcnt(4)
	v_mfma_f32_16x16x32_bf16 v[18:21], v[122:125], v[126:129], v[18:21]
	v_mfma_f32_16x16x32_bf16 v[98:101], v[122:125], v[114:117], v[98:101]
	s_setprio 0
	ds_read_b64_tr_b16 v[120:121], v166 offset:32448
	ds_read_b64_tr_b16 v[118:119], v166 offset:27840
	ds_read_b64_tr_b16 v[124:125], v166 offset:32480
	ds_read_b64_tr_b16 v[122:123], v166 offset:27872
	s_setprio 2
	s_waitcnt lgkmcnt(6)
	v_mfma_f32_16x16x32_bf16 v[94:97], v[130:133], v[114:117], v[94:97]
	v_mfma_f32_16x16x32_bf16 v[14:17], v[130:133], v[126:129], v[14:17]
	s_waitcnt lgkmcnt(4)
	v_mfma_f32_16x16x32_bf16 v[10:13], v[154:157], v[126:129], v[10:13]
	v_mfma_f32_16x16x32_bf16 v[86:89], v[154:157], v[114:117], v[86:89]
	s_setprio 0
	s_setprio 2
	s_waitcnt lgkmcnt(2)
	v_mfma_f32_16x16x32_bf16 v[70:73], v[118:121], v[114:117], v[70:73]
	v_mfma_f32_16x16x32_bf16 v[6:9], v[118:121], v[126:129], v[6:9]
	s_waitcnt lgkmcnt(0)
	v_mfma_f32_16x16x32_bf16 v[2:5], v[122:125], v[126:129], v[2:5]
	v_mfma_f32_16x16x32_bf16 v[66:69], v[122:125], v[114:117], v[66:69]
	s_setprio 0

.LBB0_1378:
	v_cmp_neq_f32_e32 vcc, s27, v171
	s_nop 1
	v_cndmask_b32_e32 v114, 0, v171, vcc
	v_sub_f32_e32 v158, v158, v114
	v_sub_f32_e32 v156, v156, v114
	v_sub_f32_e32 v154, v154, v114
	v_sub_f32_e32 v152, v152, v114
	v_sub_f32_e32 v150, v150, v114
	v_sub_f32_e32 v148, v148, v114
	v_sub_f32_e32 v146, v146, v114
	v_exp_f32_e32 v173, v158
	v_sub_f32_e32 v158, v159, v114
	v_exp_f32_e32 v175, v156
	v_sub_f32_e32 v156, v157, v114
	v_exp_f32_e32 v177, v154
	v_sub_f32_e32 v154, v155, v114
	v_exp_f32_e32 v179, v152
	v_sub_f32_e32 v152, v153, v114
	v_exp_f32_e32 v181, v150
	v_sub_f32_e32 v150, v151, v114
	v_exp_f32_e32 v183, v148
	v_sub_f32_e32 v148, v149, v114
	v_exp_f32_e32 v185, v146
	v_sub_f32_e32 v146, v147, v114
	v_sub_f32_e32 v144, v144, v114
	v_sub_f32_e32 v114, v145, v114
	v_cmp_neq_f32_e32 vcc, s27, v170
	v_exp_f32_e32 v191, v114
	v_exp_f32_e32 v159, v158
	v_cndmask_b32_e32 v114, 0, v170, vcc
	v_sub_f32_e32 v142, v142, v114
	v_exp_f32_e32 v172, v142
	v_sub_f32_e32 v142, v143, v114
	v_exp_f32_e32 v158, v142
	v_sub_f32_e32 v140, v140, v114
	v_exp_f32_e32 v174, v140
	v_sub_f32_e32 v140, v141, v114
	v_exp_f32_e32 v157, v156
	v_exp_f32_e32 v156, v140
	v_sub_f32_e32 v138, v138, v114
	v_exp_f32_e32 v176, v138
	v_sub_f32_e32 v138, v139, v114
	v_pk_add_f32 v[140:141], v[172:173], 0 op_sel_hi:[1,0]
	v_exp_f32_e32 v155, v154
	v_exp_f32_e32 v154, v138
	v_sub_f32_e32 v136, v136, v114
	v_pk_add_f32 v[140:141], v[158:159], v[140:141]
	v_exp_f32_e32 v178, v136
	v_sub_f32_e32 v136, v137, v114
	v_pk_add_f32 v[140:141], v[174:175], v[140:141]
	v_exp_f32_e32 v153, v152
	v_exp_f32_e32 v152, v136
	v_pk_add_f32 v[140:141], v[156:157], v[140:141]
	v_sub_f32_e32 v134, v134, v114
	v_pk_add_f32 v[140:141], v[176:177], v[140:141]
	v_exp_f32_e32 v180, v134
	v_sub_f32_e32 v134, v135, v114
	v_exp_f32_e32 v151, v150
	v_pk_add_f32 v[140:141], v[154:155], v[140:141]
	v_exp_f32_e32 v150, v134
	v_sub_f32_e32 v132, v132, v114
	v_pk_add_f32 v[140:141], v[178:179], v[140:141]
	v_exp_f32_e32 v182, v132
	v_sub_f32_e32 v132, v133, v114
	v_exp_f32_e32 v149, v148
	v_pk_add_f32 v[140:141], v[152:153], v[140:141]
	v_exp_f32_e32 v148, v132
	v_sub_f32_e32 v130, v130, v114
	v_sub_f32_e32 v128, v128, v114
	v_exp_f32_e32 v184, v130
	v_sub_f32_e32 v130, v131, v114
	v_exp_f32_e32 v188, v128
	v_sub_f32_e32 v114, v129, v114
	v_pk_add_f32 v[128:129], v[180:181], v[140:141]
	v_exp_f32_e32 v190, v114
	v_pk_add_f32 v[128:129], v[150:151], v[128:129]
	v_add3_u32 v114, s19, v168, v169
	v_pk_add_f32 v[128:129], v[182:183], v[128:129]
	v_exp_f32_e32 v187, v146
	v_pk_add_f32 v[128:129], v[148:149], v[128:129]
	v_exp_f32_e32 v189, v144
	v_cvt_pk_bf16_f32 v136, v173, v159
	v_cvt_pk_bf16_f32 v137, v175, v157
	v_cvt_pk_bf16_f32 v138, v177, v155
	v_cvt_pk_bf16_f32 v139, v179, v153
	v_exp_f32_e32 v186, v130
	v_pk_add_f32 v[192:193], v[184:185], v[128:129]
	v_cvt_pk_bf16_f32 v128, v181, v151
	v_cvt_pk_bf16_f32 v129, v183, v149
	v_cvt_pk_bf16_f32 v130, v185, v187
	v_cvt_pk_bf16_f32 v131, v189, v191
	v_cvt_pk_bf16_f32 v132, v172, v158
	v_cvt_pk_bf16_f32 v133, v174, v156
	v_cvt_pk_bf16_f32 v134, v176, v154
	v_cvt_pk_bf16_f32 v135, v178, v152
	v_cvt_pk_bf16_f32 v140, v180, v150
	v_cvt_pk_bf16_f32 v141, v182, v148
	v_cvt_pk_bf16_f32 v142, v184, v186
	v_cvt_pk_bf16_f32 v143, v188, v190
	ds_read_b64_tr_b16 v[144:145], v114 offset:18432
	ds_read_b64_tr_b16 v[148:149], v114 offset:18464
	ds_read_b64_tr_b16 v[152:153], v114 offset:18496
	ds_read_b64_tr_b16 v[156:157], v114 offset:18528
	ds_read_b64_tr_b16 v[146:147], v114 offset:23040
	ds_read_b64_tr_b16 v[150:151], v114 offset:23072
	ds_read_b64_tr_b16 v[154:155], v114 offset:23104
	ds_read_b64_tr_b16 v[158:159], v114 offset:23136
	v_pk_add_f32 v[172:173], v[186:187], v[192:193]
	s_nop 0
	v_pk_add_f32 v[172:173], v[188:189], v[172:173]
	s_nop 0
	v_pk_add_f32 v[172:173], v[190:191], v[172:173]
	s_nop 0
	v_pk_add_f32 v[122:123], v[122:123], v[172:173]
	s_setprio 2
	s_waitcnt lgkmcnt(3)
	v_mfma_f32_16x16x32_bf16 v[110:113], v[144:147], v[136:139], v[110:113]
	v_mfma_f32_16x16x32_bf16 v[62:65], v[144:147], v[132:135], v[62:65]
	s_waitcnt lgkmcnt(2)
	v_mfma_f32_16x16x32_bf16 v[58:61], v[148:151], v[132:135], v[58:61]
	v_mfma_f32_16x16x32_bf16 v[106:109], v[148:151], v[136:139], v[106:109]
	s_setprio 0
	ds_read_b64_tr_b16 v[146:147], v114 offset:23168
	ds_read_b64_tr_b16 v[144:145], v114 offset:18560
	ds_read_b64_tr_b16 v[150:151], v114 offset:23200
	ds_read_b64_tr_b16 v[148:149], v114 offset:18592
	s_setprio 2
	s_waitcnt lgkmcnt(5)
	v_mfma_f32_16x16x32_bf16 v[102:105], v[152:155], v[136:139], v[102:105]
	v_mfma_f32_16x16x32_bf16 v[54:57], v[152:155], v[132:135], v[54:57]
	s_waitcnt lgkmcnt(4)
	v_mfma_f32_16x16x32_bf16 v[50:53], v[156:159], v[132:135], v[50:53]
	v_mfma_f32_16x16x32_bf16 v[98:101], v[156:159], v[136:139], v[98:101]
	s_setprio 0
	ds_read_b64_tr_b16 v[154:155], v114 offset:23232
	ds_read_b64_tr_b16 v[152:153], v114 offset:18624
	ds_read_b64_tr_b16 v[158:159], v114 offset:23264
	ds_read_b64_tr_b16 v[156:157], v114 offset:18656
	s_setprio 2
	s_waitcnt lgkmcnt(6)
	v_mfma_f32_16x16x32_bf16 v[94:97], v[144:147], v[136:139], v[94:97]
	v_mfma_f32_16x16x32_bf16 v[46:49], v[144:147], v[132:135], v[46:49]
	s_waitcnt lgkmcnt(4)
	v_mfma_f32_16x16x32_bf16 v[42:45], v[148:151], v[132:135], v[42:45]
	v_mfma_f32_16x16x32_bf16 v[86:89], v[148:151], v[136:139], v[86:89]
	s_setprio 0
	ds_read_b64_tr_b16 v[146:147], v114 offset:32256
	ds_read_b64_tr_b16 v[144:145], v114 offset:27648
	ds_read_b64_tr_b16 v[150:151], v114 offset:32288
	ds_read_b64_tr_b16 v[148:149], v114 offset:27680
	s_setprio 2
	s_waitcnt lgkmcnt(6)
	v_mfma_f32_16x16x32_bf16 v[70:73], v[152:155], v[136:139], v[70:73]
	v_mfma_f32_16x16x32_bf16 v[38:41], v[152:155], v[132:135], v[38:41]
	s_waitcnt lgkmcnt(4)
	v_mfma_f32_16x16x32_bf16 v[34:37], v[156:159], v[132:135], v[34:37]
	v_mfma_f32_16x16x32_bf16 v[66:69], v[156:159], v[136:139], v[66:69]
	s_setprio 0
	ds_read_b64_tr_b16 v[134:135], v114 offset:32320
	ds_read_b64_tr_b16 v[132:133], v114 offset:27712
	ds_read_b64_tr_b16 v[138:139], v114 offset:32352
	ds_read_b64_tr_b16 v[136:137], v114 offset:27744
	s_setprio 2
	s_waitcnt lgkmcnt(6)
	v_mfma_f32_16x16x32_bf16 v[110:113], v[144:147], v[128:131], v[110:113]
	v_mfma_f32_16x16x32_bf16 v[62:65], v[144:147], v[140:143], v[62:65]
	s_waitcnt lgkmcnt(4)
	v_mfma_f32_16x16x32_bf16 v[58:61], v[148:151], v[140:143], v[58:61]
	v_mfma_f32_16x16x32_bf16 v[106:109], v[148:151], v[128:131], v[106:109]
	s_setprio 0
	ds_read_b64_tr_b16 v[146:147], v114 offset:32384
	ds_read_b64_tr_b16 v[144:145], v114 offset:27776
	ds_read_b64_tr_b16 v[150:151], v114 offset:32416
	ds_read_b64_tr_b16 v[148:149], v114 offset:27808
	s_setprio 2
	s_waitcnt lgkmcnt(6)
	v_mfma_f32_16x16x32_bf16 v[102:105], v[132:135], v[128:131], v[102:105]
	v_mfma_f32_16x16x32_bf16 v[54:57], v[132:135], v[140:143], v[54:57]
	s_waitcnt lgkmcnt(4)
	v_mfma_f32_16x16x32_bf16 v[50:53], v[136:139], v[140:143], v[50:53]
	v_mfma_f32_16x16x32_bf16 v[98:101], v[136:139], v[128:131], v[98:101]
	s_setprio 0
	ds_read_b64_tr_b16 v[134:135], v114 offset:32448
	ds_read_b64_tr_b16 v[132:133], v114 offset:27840
	ds_read_b64_tr_b16 v[138:139], v114 offset:32480
	ds_read_b64_tr_b16 v[136:137], v114 offset:27872
	s_setprio 2
	s_waitcnt lgkmcnt(6)
	v_mfma_f32_16x16x32_bf16 v[94:97], v[144:147], v[128:131], v[94:97]
	v_mfma_f32_16x16x32_bf16 v[46:49], v[144:147], v[140:143], v[46:49]
	s_waitcnt lgkmcnt(4)
	v_mfma_f32_16x16x32_bf16 v[42:45], v[148:151], v[140:143], v[42:45]
	v_mfma_f32_16x16x32_bf16 v[86:89], v[148:151], v[128:131], v[86:89]
	s_setprio 0
	s_setprio 2
	s_waitcnt lgkmcnt(2)
	v_mfma_f32_16x16x32_bf16 v[70:73], v[132:135], v[128:131], v[70:73]
	v_mfma_f32_16x16x32_bf16 v[38:41], v[132:135], v[140:143], v[38:41]
	s_waitcnt lgkmcnt(0)
	v_mfma_f32_16x16x32_bf16 v[34:37], v[136:139], v[140:143], v[34:37]
	v_mfma_f32_16x16x32_bf16 v[66:69], v[136:139], v[128:131], v[66:69]
	s_setprio 0
	s_add_u32 s22, s22, 0x20000
	s_addc_u32 s23, s23, 0
	s_cmp_lg_u32 s22, 0x80000
	s_barrier
	s_cbranch_scc0 .LBB0_1369
	s_mov_b32 s19, s18
	s_add_i32 s18, s19, 1
	s_cmp_eq_u32 s22, 0x60000
	s_cbranch_scc0 .LBB0_1373
	s_branch .LBB0_1374
